# grid barrier top counter replicated 8x (leaders add to all, a workgroup polls replica id&7): 32 pollers per word instead of 256
# speedup vs baseline: 1.0274x; 1.0044x over previous
; __device__ __forceinline__ unsigned xb_ld(unsigned* p)              { return __hip_atomic_load(p, __ATOMIC_RELAXED, __HIP_MEMORY_SCOPE_AGENT); }
; __device__ __forceinline__ unsigned xb_add(unsigned* p, unsigned v) { return __hip_atomic_fetch_add(p, v, __ATOMIC_RELAXED, __HIP_MEMORY_SCOPE_AGENT); }
; #define XB_SPIN(cond, bar) do { unsigned _sp = 0; while (cond) { __builtin_amdgcn_s_sleep(1); \
;     if ((++_sp & 255u) == 0u) { if (xb_ld(&(bar)[XB_TMO])) break; if (_sp > XB_SPIN_CAP) { atomicAdd(&(bar)[XB_TMO], 1u); break; } } } } while (0)
; __device__ __forceinline__ void xcd_barrier(const XcdBarrier& b, const int tid) {
;     ...
;         const unsigned old = xb_add(&bar[XB_XSUB(b.x)], 1u);
;         const unsigned gen = old / nloc;
;         if (old + 1u == (gen + 1u) * nloc) {
;             __builtin_amdgcn_fence(__ATOMIC_RELEASE, "agent");
;             asm volatile("s_waitcnt vmcnt(0)" ::: "memory");
;             const unsigned og = xb_add(&bar[XB_TOP], 1u);
;             const unsigned tg = og / nx;
;             if (og + 1u == (tg + 1u) * nx) xb_add(&bar[XB_TOPGEN], 1u);
;             else XB_SPIN(xb_ld(&bar[XB_TOPGEN]) == tg, bar);
.LBB0_79:
	s_or_b64 exec, exec, s[16:17]
	buffer_inv sc1
	v_cvt_f32_u32_e32 v4, v2
	s_waitcnt vmcnt(0)
	v_readfirstlane_b32 s12, v3
	v_sub_u32_e32 v3, 0, v2
	v_rcp_iflag_f32_e32 v4, v4
	v_add_u32_e32 v5, s12, v1
	v_mul_f32_e32 v4, 0x4f7ffffe, v4
	v_cvt_u32_f32_e32 v4, v4
	v_mul_lo_u32 v1, v3, v4
	v_mul_hi_u32 v1, v4, v1
	v_add_u32_e32 v1, v4, v1
	v_mul_hi_u32 v1, v5, v1
	v_mul_lo_u32 v3, v1, v2
	v_sub_u32_e32 v3, v5, v3
	v_add_u32_e32 v4, 1, v1
	v_cmp_ge_u32_e32 vcc, v3, v2
	s_nop 1
	v_cndmask_b32_e32 v1, v1, v4, vcc
	v_sub_u32_e32 v4, v3, v2
	v_cndmask_b32_e32 v3, v3, v4, vcc
	v_add_u32_e32 v4, 1, v1
	v_cmp_ge_u32_e32 vcc, v3, v2
	v_add_u32_e32 v3, 1, v5
	s_nop 0
	v_cndmask_b32_e32 v1, v1, v4, vcc
	v_mul_lo_u32 v4, v2, v1
	v_add_u32_e32 v2, v4, v2
	s_waitcnt lgkmcnt(0)
	v_add_u32_e32 v4, 1, v1
	v_mul_lo_u32 v4, v4, v0
	v_mov_b32_e32 v5, 0x3600
	v_cmp_ne_u32_e32 vcc, v3, v2
	s_cbranch_vccnz .Lgb0_wait
	buffer_wbl2 sc1
	s_waitcnt vmcnt(0) lgkmcnt(0)
	v_mov_b32_e32 v2, 1
	global_atomic_add v5, v2, s[26:27]
	global_atomic_add v5, v2, s[26:27] offset:256
	global_atomic_add v5, v2, s[26:27] offset:512
	global_atomic_add v5, v2, s[26:27] offset:768
	global_atomic_add v5, v2, s[26:27] offset:1024
	global_atomic_add v5, v2, s[26:27] offset:1280
	global_atomic_add v5, v2, s[26:27] offset:1536
	global_atomic_add v5, v2, s[26:27] offset:1792

; __device__ __forceinline__ unsigned xb_ld(unsigned* p)              { return __hip_atomic_load(p, __ATOMIC_RELAXED, __HIP_MEMORY_SCOPE_AGENT); }
; __device__ __forceinline__ unsigned xb_add(unsigned* p, unsigned v) { return __hip_atomic_fetch_add(p, v, __ATOMIC_RELAXED, __HIP_MEMORY_SCOPE_AGENT); }
; #define XB_SPIN(cond, bar) do { unsigned _sp = 0; while (cond) { __builtin_amdgcn_s_sleep(1); \
;     if ((++_sp & 255u) == 0u) { if (xb_ld(&(bar)[XB_TMO])) break; if (_sp > XB_SPIN_CAP) { atomicAdd(&(bar)[XB_TMO], 1u); break; } } } } while (0)
; __device__ __forceinline__ void xcd_barrier(const XcdBarrier& b, const int tid) {
;     ...
;             else XB_SPIN(xb_ld(&bar[XB_TOPGEN]) == tg, bar);
;             __builtin_amdgcn_fence(__ATOMIC_ACQUIRE, "agent");
;             xb_add(&bar[XB_XGEN(b.x)], 1u);
;             asm volatile("s_waitcnt vmcnt(0)" ::: "memory");
;         } else {
;             XB_SPIN(xb_ld(&bar[XB_XGEN(b.x)]) == gen, bar);
.Lgb0_spin0:
	s_and_b32 s33, s2, 7
	s_lshl_b32 s33, s33, 8
	v_add_u32_e32 v5, s33, v5
	s_mov_b32 s33, 0
.Lgb0_spin:
	global_load_dword v3, v5, s[26:27] sc1
	s_waitcnt vmcnt(0)
	v_cmp_ge_u32_e32 vcc, v3, v4
	s_cbranch_vccnz .Lgb0_done
	s_sleep 1
	s_add_i32 s33, s33, 1
	s_cmp_lt_u32 s33, 0x8000
	s_cbranch_scc1 .Lgb0_spin

; __device__ __forceinline__ unsigned xb_ld(unsigned* p)              { return __hip_atomic_load(p, __ATOMIC_RELAXED, __HIP_MEMORY_SCOPE_AGENT); }
; __device__ __forceinline__ unsigned xb_add(unsigned* p, unsigned v) { return __hip_atomic_fetch_add(p, v, __ATOMIC_RELAXED, __HIP_MEMORY_SCOPE_AGENT); }
; #define XB_SPIN(cond, bar) do { unsigned _sp = 0; while (cond) { __builtin_amdgcn_s_sleep(1); \
;     if ((++_sp & 255u) == 0u) { if (xb_ld(&(bar)[XB_TMO])) break; if (_sp > XB_SPIN_CAP) { atomicAdd(&(bar)[XB_TMO], 1u); break; } } } } while (0)
; __device__ __forceinline__ void xcd_barrier(const XcdBarrier& b, const int tid) {
;     ...
;         const unsigned old = xb_add(&bar[XB_XSUB(b.x)], 1u);
;         const unsigned gen = old / nloc;
;         if (old + 1u == (gen + 1u) * nloc) {
;             __builtin_amdgcn_fence(__ATOMIC_RELEASE, "agent");
;             asm volatile("s_waitcnt vmcnt(0)" ::: "memory");
;             const unsigned og = xb_add(&bar[XB_TOP], 1u);
;             const unsigned tg = og / nx;
;             if (og + 1u == (tg + 1u) * nx) xb_add(&bar[XB_TOPGEN], 1u);
;             else XB_SPIN(xb_ld(&bar[XB_TOPGEN]) == tg, bar);
.LBB0_169:
	s_or_b64 exec, exec, s[22:23]
	buffer_inv sc1
	v_cvt_f32_u32_e32 v4, v2
	s_waitcnt vmcnt(0)
	v_readfirstlane_b32 s20, v3
	v_sub_u32_e32 v3, 0, v2
	v_rcp_iflag_f32_e32 v4, v4
	v_add_u32_e32 v5, s20, v1
	v_mul_f32_e32 v4, 0x4f7ffffe, v4
	v_cvt_u32_f32_e32 v4, v4
	v_mul_lo_u32 v1, v3, v4
	v_mul_hi_u32 v1, v4, v1
	v_add_u32_e32 v1, v4, v1
	v_mul_hi_u32 v1, v5, v1
	v_mul_lo_u32 v3, v1, v2
	v_sub_u32_e32 v3, v5, v3
	v_add_u32_e32 v4, 1, v1
	v_cmp_ge_u32_e32 vcc, v3, v2
	s_nop 1
	v_cndmask_b32_e32 v1, v1, v4, vcc
	v_sub_u32_e32 v4, v3, v2
	v_cndmask_b32_e32 v3, v3, v4, vcc
	v_add_u32_e32 v4, 1, v1
	v_cmp_ge_u32_e32 vcc, v3, v2
	v_add_u32_e32 v3, 1, v5
	s_nop 0
	v_cndmask_b32_e32 v1, v1, v4, vcc
	v_mul_lo_u32 v4, v2, v1
	v_add_u32_e32 v2, v4, v2
	s_waitcnt lgkmcnt(0)
	v_add_u32_e32 v4, 1, v1
	v_mul_lo_u32 v4, v4, v0
	v_mov_b32_e32 v5, 0x3600
	v_cmp_ne_u32_e32 vcc, v3, v2
	s_cbranch_vccnz .Lgb1_out
	buffer_wbl2 sc1
	s_waitcnt vmcnt(0) lgkmcnt(0)
	v_mov_b32_e32 v2, 1
	global_atomic_add v5, v2, s[26:27]
	global_atomic_add v5, v2, s[26:27] offset:256
	global_atomic_add v5, v2, s[26:27] offset:512
	global_atomic_add v5, v2, s[26:27] offset:768
	global_atomic_add v5, v2, s[26:27] offset:1024
	global_atomic_add v5, v2, s[26:27] offset:1280
	global_atomic_add v5, v2, s[26:27] offset:1536
	global_atomic_add v5, v2, s[26:27] offset:1792

; __device__ __forceinline__ unsigned xb_ld(unsigned* p)              { return __hip_atomic_load(p, __ATOMIC_RELAXED, __HIP_MEMORY_SCOPE_AGENT); }
; __device__ __forceinline__ unsigned xb_add(unsigned* p, unsigned v) { return __hip_atomic_fetch_add(p, v, __ATOMIC_RELAXED, __HIP_MEMORY_SCOPE_AGENT); }
; #define XB_SPIN(cond, bar) do { unsigned _sp = 0; while (cond) { __builtin_amdgcn_s_sleep(1); \
;     if ((++_sp & 255u) == 0u) { if (xb_ld(&(bar)[XB_TMO])) break; if (_sp > XB_SPIN_CAP) { atomicAdd(&(bar)[XB_TMO], 1u); break; } } } } while (0)
; __device__ __forceinline__ void xcd_barrier(const XcdBarrier& b, const int tid) {
;     ...
;             else XB_SPIN(xb_ld(&bar[XB_TOPGEN]) == tg, bar);
;             __builtin_amdgcn_fence(__ATOMIC_ACQUIRE, "agent");
;             xb_add(&bar[XB_XGEN(b.x)], 1u);
;             asm volatile("s_waitcnt vmcnt(0)" ::: "memory");
;         } else {
;             XB_SPIN(xb_ld(&bar[XB_XGEN(b.x)]) == gen, bar);
; __global__ void __launch_bounds__(512, 2) hymba_fwd(Args args) {
;     ...
;             for (int hs = 0; hs < 2 * nsteps; ++hs) {
;                 const bool doA = (((hs & 1) == 0) == (wave < 4));
;                 if (doA) { if (ia < nA) { const int a = bx + ia * G; const int blk = a >> 4, h = a & 15;
;                         attn_wave(Qb, Kb, Vb, MIX, h, 256 * blk + wave, vbuf, btab + h * 396, lane); ++ia; } }
.LBB0_214:
	s_and_b32 s0, s83, 1
	v_cmp_ne_u32_e32 vcc, s0, v223
	s_mov_b64 s[6:7], -1
	s_cbranch_vccnz .LBB0_234
	s_cmp_ge_i32 s82, s69
	s_mov_b32 s0, s82
	s_cbranch_scc1 .LBB0_233
	s_cmp_lg_u32 s98, 0
	s_cbranch_scc1 .Lp2gb_passed
	s_mov_b32 s99, 0
	s_cmp_lg_u32 s92, 0
	s_cbranch_scc1 .Lp2gb_follow
	v_mov_b32_e32 v21, 0x22604
	ds_read_b32 v233, v21
	v_mov_b32_e32 v21, 0x3600
	s_and_b32 s99, s2, 7
	s_lshl_b32 s99, s99, 8
	v_add_u32_e32 v21, s99, v21
	s_mov_b32 s99, 0
	global_load_dword v22, v21, s[26:27] sc1
	s_waitcnt vmcnt(0) lgkmcnt(0)
	v_mul_u32_u24_e32 v233, 2, v233
	s_branch .Lp2gb_chk
.Lp2gb_spin:
	s_sleep 1
	global_load_dword v22, v21, s[26:27] sc1
	s_waitcnt vmcnt(0)

; __device__ __forceinline__ unsigned xb_ld(unsigned* p)              { return __hip_atomic_load(p, __ATOMIC_RELAXED, __HIP_MEMORY_SCOPE_AGENT); }
; __device__ __forceinline__ unsigned xb_add(unsigned* p, unsigned v) { return __hip_atomic_fetch_add(p, v, __ATOMIC_RELAXED, __HIP_MEMORY_SCOPE_AGENT); }
; #define XB_SPIN(cond, bar) do { unsigned _sp = 0; while (cond) { __builtin_amdgcn_s_sleep(1); \
;     if ((++_sp & 255u) == 0u) { if (xb_ld(&(bar)[XB_TMO])) break; if (_sp > XB_SPIN_CAP) { atomicAdd(&(bar)[XB_TMO], 1u); break; } } } } while (0)
; __device__ __forceinline__ void xcd_barrier(const XcdBarrier& b, const int tid) {
;     ...
;         const unsigned old = xb_add(&bar[XB_XSUB(b.x)], 1u);
;         const unsigned gen = old / nloc;
;         if (old + 1u == (gen + 1u) * nloc) {
;             __builtin_amdgcn_fence(__ATOMIC_RELEASE, "agent");
;             asm volatile("s_waitcnt vmcnt(0)" ::: "memory");
;             const unsigned og = xb_add(&bar[XB_TOP], 1u);
;             const unsigned tg = og / nx;
;             if (og + 1u == (tg + 1u) * nx) xb_add(&bar[XB_TOPGEN], 1u);
;             else XB_SPIN(xb_ld(&bar[XB_TOPGEN]) == tg, bar);
.LBB0_433:
	s_or_b64 exec, exec, s[12:13]
	buffer_inv sc1
	v_cvt_f32_u32_e32 v4, v2
	s_waitcnt vmcnt(0)
	v_readfirstlane_b32 s6, v3
	v_sub_u32_e32 v3, 0, v2
	v_rcp_iflag_f32_e32 v4, v4
	v_add_u32_e32 v5, s6, v1
	v_mul_f32_e32 v4, 0x4f7ffffe, v4
	v_cvt_u32_f32_e32 v4, v4
	v_mul_lo_u32 v1, v3, v4
	v_mul_hi_u32 v1, v4, v1
	v_add_u32_e32 v1, v4, v1
	v_mul_hi_u32 v1, v5, v1
	v_mul_lo_u32 v3, v1, v2
	v_sub_u32_e32 v3, v5, v3
	v_add_u32_e32 v4, 1, v1
	v_cmp_ge_u32_e32 vcc, v3, v2
	s_nop 1
	v_cndmask_b32_e32 v1, v1, v4, vcc
	v_sub_u32_e32 v4, v3, v2
	v_cndmask_b32_e32 v3, v3, v4, vcc
	v_add_u32_e32 v4, 1, v1
	v_cmp_ge_u32_e32 vcc, v3, v2
	v_add_u32_e32 v3, 1, v5
	s_nop 0
	v_cndmask_b32_e32 v1, v1, v4, vcc
	v_mul_lo_u32 v4, v2, v1
	v_add_u32_e32 v2, v4, v2
	s_waitcnt lgkmcnt(0)
	v_add_u32_e32 v4, 1, v1
	v_mul_lo_u32 v4, v4, v0
	v_mov_b32_e32 v5, 0x3600
	v_cmp_ne_u32_e32 vcc, v3, v2
	s_cbranch_vccnz .Lgb2_wait
	buffer_wbl2 sc1
	s_waitcnt vmcnt(0) lgkmcnt(0)
	v_mov_b32_e32 v2, 1
	global_atomic_add v5, v2, s[26:27]
	global_atomic_add v5, v2, s[26:27] offset:256
	global_atomic_add v5, v2, s[26:27] offset:512
	global_atomic_add v5, v2, s[26:27] offset:768
	global_atomic_add v5, v2, s[26:27] offset:1024
	global_atomic_add v5, v2, s[26:27] offset:1280
	global_atomic_add v5, v2, s[26:27] offset:1536
	global_atomic_add v5, v2, s[26:27] offset:1792

; __device__ __forceinline__ unsigned xb_ld(unsigned* p)              { return __hip_atomic_load(p, __ATOMIC_RELAXED, __HIP_MEMORY_SCOPE_AGENT); }
; __device__ __forceinline__ unsigned xb_add(unsigned* p, unsigned v) { return __hip_atomic_fetch_add(p, v, __ATOMIC_RELAXED, __HIP_MEMORY_SCOPE_AGENT); }
; #define XB_SPIN(cond, bar) do { unsigned _sp = 0; while (cond) { __builtin_amdgcn_s_sleep(1); \
;     if ((++_sp & 255u) == 0u) { if (xb_ld(&(bar)[XB_TMO])) break; if (_sp > XB_SPIN_CAP) { atomicAdd(&(bar)[XB_TMO], 1u); break; } } } } while (0)
; __device__ __forceinline__ void xcd_barrier(const XcdBarrier& b, const int tid) {
;     ...
;         const unsigned old = xb_add(&bar[XB_XSUB(b.x)], 1u);
;         const unsigned gen = old / nloc;
;         if (old + 1u == (gen + 1u) * nloc) {
;             __builtin_amdgcn_fence(__ATOMIC_RELEASE, "agent");
;             asm volatile("s_waitcnt vmcnt(0)" ::: "memory");
;             const unsigned og = xb_add(&bar[XB_TOP], 1u);
;             const unsigned tg = og / nx;
;             if (og + 1u == (tg + 1u) * nx) xb_add(&bar[XB_TOPGEN], 1u);
;             else XB_SPIN(xb_ld(&bar[XB_TOPGEN]) == tg, bar);
.LBB0_512:
	s_or_b64 exec, exec, s[8:9]
	buffer_inv sc1
	v_cvt_f32_u32_e32 v4, v2
	s_waitcnt vmcnt(0)
	v_readfirstlane_b32 s6, v3
	v_sub_u32_e32 v3, 0, v2
	v_rcp_iflag_f32_e32 v4, v4
	v_add_u32_e32 v5, s6, v1
	v_mul_f32_e32 v4, 0x4f7ffffe, v4
	v_cvt_u32_f32_e32 v4, v4
	v_mul_lo_u32 v1, v3, v4
	v_mul_hi_u32 v1, v4, v1
	v_add_u32_e32 v1, v4, v1
	v_mul_hi_u32 v1, v5, v1
	v_mul_lo_u32 v3, v1, v2
	v_sub_u32_e32 v3, v5, v3
	v_add_u32_e32 v4, 1, v1
	v_cmp_ge_u32_e32 vcc, v3, v2
	s_nop 1
	v_cndmask_b32_e32 v1, v1, v4, vcc
	v_sub_u32_e32 v4, v3, v2
	v_cndmask_b32_e32 v3, v3, v4, vcc
	v_add_u32_e32 v4, 1, v1
	v_cmp_ge_u32_e32 vcc, v3, v2
	v_add_u32_e32 v3, 1, v5
	s_nop 0
	v_cndmask_b32_e32 v1, v1, v4, vcc
	v_mul_lo_u32 v4, v2, v1
	v_add_u32_e32 v2, v4, v2
	s_waitcnt lgkmcnt(0)
	v_add_u32_e32 v4, 1, v1
	v_mul_lo_u32 v4, v4, v0
	v_mov_b32_e32 v5, 0x3600
	v_cmp_ne_u32_e32 vcc, v3, v2
	s_cbranch_vccnz .Lgb3_wait
	buffer_wbl2 sc1
	s_waitcnt vmcnt(0) lgkmcnt(0)
	v_mov_b32_e32 v2, 1
	global_atomic_add v5, v2, s[26:27]
	global_atomic_add v5, v2, s[26:27] offset:256
	global_atomic_add v5, v2, s[26:27] offset:512
	global_atomic_add v5, v2, s[26:27] offset:768
	global_atomic_add v5, v2, s[26:27] offset:1024
	global_atomic_add v5, v2, s[26:27] offset:1280
	global_atomic_add v5, v2, s[26:27] offset:1536
	global_atomic_add v5, v2, s[26:27] offset:1792

; __device__ __forceinline__ unsigned xb_ld(unsigned* p)              { return __hip_atomic_load(p, __ATOMIC_RELAXED, __HIP_MEMORY_SCOPE_AGENT); }
; __device__ __forceinline__ unsigned xb_add(unsigned* p, unsigned v) { return __hip_atomic_fetch_add(p, v, __ATOMIC_RELAXED, __HIP_MEMORY_SCOPE_AGENT); }
; #define XB_SPIN(cond, bar) do { unsigned _sp = 0; while (cond) { __builtin_amdgcn_s_sleep(1); \
;     if ((++_sp & 255u) == 0u) { if (xb_ld(&(bar)[XB_TMO])) break; if (_sp > XB_SPIN_CAP) { atomicAdd(&(bar)[XB_TMO], 1u); break; } } } } while (0)
; __device__ __forceinline__ void xcd_barrier(const XcdBarrier& b, const int tid) {
;     ...
;         const unsigned old = xb_add(&bar[XB_XSUB(b.x)], 1u);
;         const unsigned gen = old / nloc;
;         if (old + 1u == (gen + 1u) * nloc) {
;             __builtin_amdgcn_fence(__ATOMIC_RELEASE, "agent");
;             asm volatile("s_waitcnt vmcnt(0)" ::: "memory");
;             const unsigned og = xb_add(&bar[XB_TOP], 1u);
;             const unsigned tg = og / nx;
;             if (og + 1u == (tg + 1u) * nx) xb_add(&bar[XB_TOPGEN], 1u);
;             else XB_SPIN(xb_ld(&bar[XB_TOPGEN]) == tg, bar);
;             __builtin_amdgcn_fence(__ATOMIC_ACQUIRE, "agent");
;             xb_add(&bar[XB_XGEN(b.x)], 1u);
;             asm volatile("s_waitcnt vmcnt(0)" ::: "memory");
;         } else {
;             XB_SPIN(xb_ld(&bar[XB_XGEN(b.x)]) == gen, bar);
.LBB0_802:
	s_or_b64 exec, exec, s[10:11]
	buffer_inv sc1
	v_cvt_f32_u32_e32 v4, v2
	s_waitcnt vmcnt(0)
	v_readfirstlane_b32 s8, v3
	v_sub_u32_e32 v3, 0, v2
	v_rcp_iflag_f32_e32 v4, v4
	v_add_u32_e32 v5, s8, v1
	v_mul_f32_e32 v4, 0x4f7ffffe, v4
	v_cvt_u32_f32_e32 v4, v4
	v_mul_lo_u32 v1, v3, v4
	v_mul_hi_u32 v1, v4, v1
	v_add_u32_e32 v1, v4, v1
	v_mul_hi_u32 v1, v5, v1
	v_mul_lo_u32 v3, v1, v2
	v_sub_u32_e32 v3, v5, v3
	v_add_u32_e32 v4, 1, v1
	v_cmp_ge_u32_e32 vcc, v3, v2
	s_nop 1
	v_cndmask_b32_e32 v1, v1, v4, vcc
	v_sub_u32_e32 v4, v3, v2
	v_cndmask_b32_e32 v3, v3, v4, vcc
	v_add_u32_e32 v4, 1, v1
	v_cmp_ge_u32_e32 vcc, v3, v2
	v_add_u32_e32 v3, 1, v5
	s_nop 0
	v_cndmask_b32_e32 v1, v1, v4, vcc
	v_mul_lo_u32 v4, v2, v1
	v_add_u32_e32 v2, v4, v2
	s_waitcnt lgkmcnt(0)
	v_add_u32_e32 v4, 1, v1
	v_mul_lo_u32 v4, v4, v0
	v_mov_b32_e32 v5, 0x3600
	v_cmp_ne_u32_e32 vcc, v3, v2
	s_cbranch_vccnz .Lgb5_wait
	buffer_wbl2 sc1
	s_waitcnt vmcnt(0) lgkmcnt(0)
	v_mov_b32_e32 v2, 1
	global_atomic_add v5, v2, s[26:27]
	global_atomic_add v5, v2, s[26:27] offset:256
	global_atomic_add v5, v2, s[26:27] offset:512
	global_atomic_add v5, v2, s[26:27] offset:768
	global_atomic_add v5, v2, s[26:27] offset:1024
	global_atomic_add v5, v2, s[26:27] offset:1280
	global_atomic_add v5, v2, s[26:27] offset:1536
	global_atomic_add v5, v2, s[26:27] offset:1792
.Lgb5_wait:
	s_and_b32 s28, s2, 7
	s_lshl_b32 s28, s28, 8
	v_add_u32_e32 v5, s28, v5
	s_mov_b32 s28, 0
.Lgb5_spin:
	global_load_dword v3, v5, s[26:27] sc1
	s_waitcnt vmcnt(0)
	v_cmp_ge_u32_e32 vcc, v3, v4
	s_cbranch_vccnz .Lgb5_done
	s_sleep 1
	s_add_i32 s28, s28, 1
	s_cmp_lt_u32 s28, 0x8000
	s_cbranch_scc1 .Lgb5_spin

; __device__ __forceinline__ unsigned xb_ld(unsigned* p)              { return __hip_atomic_load(p, __ATOMIC_RELAXED, __HIP_MEMORY_SCOPE_AGENT); }
; __device__ __forceinline__ unsigned xb_add(unsigned* p, unsigned v) { return __hip_atomic_fetch_add(p, v, __ATOMIC_RELAXED, __HIP_MEMORY_SCOPE_AGENT); }
; #define XB_SPIN(cond, bar) do { unsigned _sp = 0; while (cond) { __builtin_amdgcn_s_sleep(1); \
;     if ((++_sp & 255u) == 0u) { if (xb_ld(&(bar)[XB_TMO])) break; if (_sp > XB_SPIN_CAP) { atomicAdd(&(bar)[XB_TMO], 1u); break; } } } } while (0)
; __device__ __forceinline__ void xcd_barrier(const XcdBarrier& b, const int tid) {
;     ...
;             else XB_SPIN(xb_ld(&bar[XB_TOPGEN]) == tg, bar);
;             __builtin_amdgcn_fence(__ATOMIC_ACQUIRE, "agent");
;             xb_add(&bar[XB_XGEN(b.x)], 1u);
;             asm volatile("s_waitcnt vmcnt(0)" ::: "memory");
;         } else {
;             XB_SPIN(xb_ld(&bar[XB_XGEN(b.x)]) == gen, bar);
; __global__ void __launch_bounds__(512, 2) hymba_fwd(Args args) {
;     ...
;             for (int tq = gw; tq < SEQ; tq += 4 * NGW) {
;             int cc0[4], cc1[4];
; #pragma unroll
;             for (int k = 0; k < 4; ++k) { const int t = tq + k * NGW; cc0[k] = 0; cc1[k] = 0; if (t < SEQ) { cc0[k] = tokpos[2 * t]; cc1[k] = tokpos[2 * t + 1]; } }
;             v2u xb[2][8]; unsigned b0[2][8], b1[2][8];
;             auto ld = [&](int k) { const int t = tq + k * NGW; const int c0 = cc0[k], c1 = cc1[k];
;                 const size_t r0 = (size_t)(256 * tb[c0 >> 16] + (c0 & 0xffff)), r1 = (size_t)(256 * tb[c1 >> 16] + (c1 & 0xffff));
.LBB0_913:
	s_ashr_i32 s3, s2, 31
	s_lshl_b64 s[0:1], s[2:3], 2
	s_add_u32 s0, s19, s0
	s_addc_u32 s1, s30, s1
	global_load_dwordx2 v[26:27], v48, s[0:1]
	s_cmp_lg_u32 s98, 0
	s_cbranch_scc1 .Lp7gb_passed
	s_mov_b32 s99, 0
	s_cmp_lg_u32 s92, 0
	s_cbranch_scc1 .Lp7gb_follow
	v_mov_b32_e32 v100, 0x22604
	ds_read_b32 v101, v100
	v_mov_b32_e32 v100, 0x3600
	s_and_b32 s99, s2, 7
	s_lshl_b32 s99, s99, 8
	v_add_u32_e32 v100, s99, v100
	s_mov_b32 s99, 0
	global_load_dword v102, v100, s[26:27] sc1
	s_waitcnt vmcnt(0) lgkmcnt(0)
	v_mul_u32_u24_e32 v101, 6, v101
	s_branch .Lp7gb_chk
.Lp7gb_spin:
	s_sleep 1
	global_load_dword v102, v100, s[26:27] sc1
	s_waitcnt vmcnt(0)
